# P4 scans: RWKV a4 unpack moved to back-edge (no vmcnt(0) inside next-chunk prefetch), mLSTM g3 prefetch into fresh regs (no vmcnt(0) after prefetch)
# speedup vs baseline: 1.0168x; 1.0168x over previous
; #define LAS __attribute__((address_space(3)))
; __device__ __forceinline__ void mlstm_scan_unit(Frame& F, int unit, LAS unsigned* bcnt, unsigned& btarget) {
;     ...
;     for (int ch = 0; ch < SEQ / 64; ++ch) {
;         const size_t tk0 = (size_t)b * SEQ + ch * 64;
;         LAS bf16* cTc = LcT + (ch & 1) * 48 * 136; LAS bf16* cTn = LcT + ((ch + 1) & 1) * 48 * 136;
;         float mnew, dec;
;         { const float bc = g3[0], u = g3[1], pm = g3[2];
;           const float gtot = __shfl(bc, 63), pmall = __shfl(pm, 63);
.LBB0_922:
	s_waitcnt vmcnt(0)
	v_mov_b32_e32 v38, v244
	v_mov_b32_e32 v39, v245
	v_mov_b32_e32 v40, v246
	s_cmp_lg_u32 s70, 32
	v_mov_b32_e32 v127, v93
	s_mov_b32 s71, s70
	s_cbranch_scc0 .LBB0_909

; #define LAS __attribute__((address_space(3)))
; #define LDS_WAIT() asm volatile("s_waitcnt lgkmcnt(0)" ::: "memory")
; __device__ __forceinline__ unsigned pk2(float lo, float hi) { const f32x2 v = {lo, hi}; const bf16x2_t b = __builtin_convertvector(v, bf16x2_t); return __builtin_bit_cast(unsigned, b); }
; __device__ __forceinline__ void rw_bar(LAS unsigned* cnt, unsigned& target, int lane) {
;     asm volatile("s_waitcnt lgkmcnt(0)" ::: "memory");
;     if (lane == 0) __hip_atomic_fetch_add(cnt, 1u, __ATOMIC_RELAXED, __HIP_MEMORY_SCOPE_WORKGROUP);
; __device__ __forceinline__ void mlstm_scan_unit(Frame& F, int unit, LAS unsigned* bcnt, unsigned& btarget) {
;     ...
;         for (int i = 0; i < 4; ++i) { *(LAS v4u*)(Lq + (pr0 + 16 * i) * 136 + pc) = rq[i]; *(LAS v4u*)(Lk + (pr0 + 16 * i) * 136 + pc) = rk[i]; }
;         LDS_WAIT();
;         { const int j = tid >> 2, d0 = 8 * (tid & 3); const float wkj = swk[j]; *(LAS v4u*)(Lv + j * VS + d0) = rv;
;           const unsigned uu[4] = {rv.x, rv.y, rv.z, rv.w}; v4u sv;
;           sv.x = pk2(wkj * __uint_as_float(uu[0] << 16), wkj * __uint_as_float(uu[0] & 0xffff0000u)); sv.y = pk2(wkj * __uint_as_float(uu[1] << 16), wkj * __uint_as_float(uu[1] & 0xffff0000u));
;           sv.z = pk2(wkj * __uint_as_float(uu[2] << 16), wkj * __uint_as_float(uu[2] & 0xffff0000u)); sv.w = pk2(wkj * __uint_as_float(uu[3] << 16), wkj * __uint_as_float(uu[3] & 0xffff0000u));
;           *(LAS v4u*)(Lvs + j * VS + d0) = sv; }
;         if (ch + 1 < SEQ / 64) ML_LOAD(ch + 1);
.LBB0_925:
	ds_write_b128 v113, v[2:5] offset:45056
	ds_write_b128 v113, v[6:9] offset:62464
	ds_write_b128 v113, v[10:13] offset:49408
	ds_write_b128 v114, v[14:17] offset:4352
	ds_write_b128 v113, v[18:21] offset:53760
	ds_write_b128 v114, v[22:25] offset:8704
	ds_write_b128 v113, v[26:29] offset:58112
	ds_write_b128 v114, v[30:33] offset:13056
	s_waitcnt lgkmcnt(0)
	ds_read_b32 v72, v105
	v_lshlrev_b32_e32 v68, 16, v34
	v_and_b32_e32 v69, 0xffff0000, v34
	v_lshlrev_b32_e32 v70, 16, v35
	v_and_b32_e32 v71, 0xffff0000, v35
	s_waitcnt lgkmcnt(0)
	v_pk_mul_f32 v[68:69], v[72:73], v[68:69] op_sel_hi:[0,1]
	v_pk_mul_f32 v[70:71], v[72:73], v[70:71] op_sel_hi:[0,1]
	v_cvt_pk_bf16_f32 v68, v68, v69
	v_cvt_pk_bf16_f32 v69, v70, v71
	v_lshlrev_b32_e32 v70, 16, v36
	v_and_b32_e32 v71, 0xffff0000, v36
	v_lshlrev_b32_e32 v74, 16, v37
	v_and_b32_e32 v75, 0xffff0000, v37
	s_add_i32 s70, s71, 1
	v_pk_mul_f32 v[70:71], v[72:73], v[70:71] op_sel_hi:[0,1]
	v_pk_mul_f32 v[72:73], v[72:73], v[74:75] op_sel_hi:[0,1]
	v_cvt_pk_bf16_f32 v70, v70, v71
	v_cvt_pk_bf16_f32 v71, v72, v73
	s_cmp_eq_u32 s71, 31
	ds_write_b128 v106, v[34:37]
	ds_write_b128 v107, v[68:71]
	s_cbranch_scc1 .LBB0_927
	s_lshl_b32 s0, s70, 6
	s_add_u32 s58, s50, s0
	s_addc_u32 s59, s51, 0
	v_lshl_add_u64 v[2:3], s[58:59], 0, v[80:81]
	v_lshlrev_b64 v[2:3], 11, v[2:3]
	v_lshl_add_u64 v[26:27], v[94:95], 0, v[2:3]
	v_add_co_u32_e32 v14, vcc, 0x8000, v26
	v_lshl_add_u64 v[34:35], s[58:59], 0, v[86:87]
	v_mov_b64_e32 v[36:37], s[2:3]
	v_addc_co_u32_e32 v15, vcc, 0, v27, vcc
	v_mad_u64_u32 v[36:37], s[60:61], v34, s66, v[36:37]
	v_add_co_u32_e32 v22, vcc, 0x10000, v26
	v_mad_i32_i24 v37, v35, s66, v37
	s_lshl_b32 s0, s52, 1
	v_addc_co_u32_e32 v23, vcc, 0, v27, vcc
	v_lshl_add_u64 v[34:35], v[36:37], 0, s[0:1]
	s_mov_b32 s55, s1
	v_add_co_u32_e32 v30, vcc, 0x18000, v26
	v_lshl_add_u64 v[34:35], v[34:35], 0, s[54:55]
	s_nop 0
	v_addc_co_u32_e32 v31, vcc, 0, v27, vcc
	v_lshl_add_u64 v[34:35], v[34:35], 0, v[82:83]
	v_mov_b32_e32 v37, s59
	v_or_b32_e32 v36, s58, v162
	v_add_co_u32_e32 v34, vcc, 0x2000, v34
	v_lshlrev_b64 v[36:37], 6, v[36:37]
	s_nop 0
	v_addc_co_u32_e32 v35, vcc, 0, v35, vcc
	v_lshl_add_u64 v[38:39], s[56:57], 0, v[36:37]
	global_load_dwordx4 v[2:5], v[26:27], off
	global_load_dwordx4 v[6:9], v[26:27], off offset:1024
	global_load_dwordx4 v[10:13], v[14:15], off
	s_nop 0
	global_load_dwordx4 v[14:17], v[14:15], off offset:1024
	s_nop 0
	global_load_dwordx4 v[18:21], v[22:23], off
	s_nop 0
	global_load_dwordx4 v[22:25], v[22:23], off offset:1024
	s_nop 0
	global_load_dwordx4 v[26:29], v[30:31], off
	s_nop 0
	global_load_dwordx4 v[30:33], v[30:31], off offset:1024
	s_nop 0
	global_load_dwordx4 v[34:37], v[34:35], off offset:896
	s_nop 0
	global_load_dwordx4 v[244:247], v[38:39], off
.LBB0_927:
	s_waitcnt lgkmcnt(0)
	s_and_saveexec_b64 s[58:59], s[4:5]
	s_cbranch_execz .LBB0_930
	s_mov_b64 s[60:61], exec
	v_mbcnt_lo_u32_b32 v41, s60, 0
	v_mbcnt_hi_u32_b32 v41, s61, v41
	v_cmp_eq_u32_e32 vcc, 0, v41
	s_and_b64 s[62:63], exec, vcc
	s_mov_b64 exec, s[62:63]
	s_bcnt1_i32_b64 s0, s[60:61]
	v_mov_b32_e32 v41, s67
	v_mov_b32_e32 v67, s0
	ds_add_u32 v41, v67

; #define LAS __attribute__((address_space(3)))
; __device__ __forceinline__ unsigned long long pack4bf(f32x4 v) { return (unsigned long long)pk2(v[0], v[1]) | ((unsigned long long)pk2(v[2], v[3]) << 32); }
; __device__ __forceinline__ void rw_bar(LAS unsigned* cnt, unsigned& target, int lane) {
;     asm volatile("s_waitcnt lgkmcnt(0)" ::: "memory");
;     if (lane == 0) __hip_atomic_fetch_add(cnt, 1u, __ATOMIC_RELAXED, __HIP_MEMORY_SCOPE_WORKGROUP);
;     target += 4u;
;     while ((unsigned)__builtin_amdgcn_readfirstlane((int)__hip_atomic_load(cnt, __ATOMIC_RELAXED, __HIP_MEMORY_SCOPE_WORKGROUP)) < target) __builtin_amdgcn_s_sleep(1);
; __device__ __forceinline__ void mlstm_scan_unit(Frame& F, int unit, LAS unsigned* bcnt, unsigned& btarget) {
;     ...
;         { const int tt = w; const int t = 16 * tt + fr; const float mxt = smx[t];
; #pragma unroll
;           for (int jt = 0; jt < 4; ++jt) { f32x4 acc = (f32x4){0.f, 0.f, 0.f, 0.f};
;               if (jt <= tt) {
; #pragma unroll
;                   for (int ks = 0; ks < 4; ++ks) { const s16x8 a = *(const LAS s16x8*)(Lk + (16 * jt + fr) * 136 + 32 * ks + 8 * fq), bq = *(const LAS s16x8*)(Lq + (16 * tt + fr) * 136 + 32 * ks + 8 * fq);
;                       acc = __builtin_amdgcn_mfma_f32_16x16x32_bf16(a, bq, acc, 0, 0, 0); }
;                   const f32x4 u4 = *(const LAS f32x4*)(su + 16 * jt + 4 * fq);
; #pragma unroll
;                   for (int rg_ = 0; rg_ < 4; ++rg_) { const int j = 16 * jt + 4 * fq + rg_; acc[rg_] = (j <= t) ? acc[rg_] * __expf(u4[rg_] - mxt) : 0.f; } }
;               *(LAS unsigned long long*)(Ls + t * 72 + 16 * jt + 4 * fq) = pack4bf(acc); } }
.LBB0_932:
	v_mov_b32_e32 v41, s67
	ds_read_b32 v41, v41
	s_mov_b64 s[58:59], -1
	s_waitcnt lgkmcnt(0)
	v_readfirstlane_b32 s55, v41
	s_cmp_ge_u32 s55, s0
	s_cbranch_scc1 .LBB0_931
	s_mov_b64 s[58:59], 0
	s_sleep 1
	s_branch .LBB0_931
.LBB0_934:
	ds_read_b32 v41, v108
	ds_read_b128 v[68:71], v115 offset:62464
	ds_read_b128 v[72:75], v88 offset:45056
	s_mov_b32 s0, 0x5040100
	s_and_b64 vcc, exec, s[44:45]
	s_waitcnt lgkmcnt(0)
	v_mfma_f32_16x16x32_bf16 v[68:71], v[68:71], v[72:75], 0
	ds_read_b128 v[72:75], v115 offset:62528
	ds_read_b128 v[128:131], v88 offset:45120
	s_waitcnt lgkmcnt(0)
	v_mfma_f32_16x16x32_bf16 v[68:71], v[72:75], v[128:131], v[68:71]
	ds_read_b128 v[72:75], v115 offset:62592
	ds_read_b128 v[128:131], v88 offset:45184
	s_waitcnt lgkmcnt(0)
	v_mfma_f32_16x16x32_bf16 v[68:71], v[72:75], v[128:131], v[68:71]
	ds_read_b128 v[72:75], v115 offset:62656
	ds_read_b128 v[128:131], v88 offset:45248
	s_waitcnt lgkmcnt(0)
	v_mfma_f32_16x16x32_bf16 v[68:71], v[72:75], v[128:131], v[68:71]
	ds_read_b128 v[72:75], v89
	s_waitcnt lgkmcnt(0)
	v_sub_f32_e32 v67, v72, v41
	v_mul_f32_e32 v67, 0x3fb8aa3b, v67
	v_exp_f32_e32 v67, v67
	s_nop 2
	v_mul_f32_e32 v67, v68, v67
	v_sub_f32_e32 v68, v73, v41
	v_mul_f32_e32 v68, 0x3fb8aa3b, v68
	v_exp_f32_e32 v68, v68
	v_cndmask_b32_e64 v67, v67, 0, s[6:7]
	v_mul_f32_e32 v68, v69, v68
	v_cndmask_b32_e64 v72, 0, v68, s[8:9]
	v_sub_f32_e32 v68, v74, v41
	v_sub_f32_e32 v69, v75, v41
	v_mul_f32_e32 v68, 0x3fb8aa3b, v68
	v_mul_f32_e32 v69, 0x3fb8aa3b, v69
	v_exp_f32_e32 v68, v68
	v_exp_f32_e32 v69, v69
	s_nop 0
	v_pk_mul_f32 v[68:69], v[70:71], v[68:69]
	v_cvt_pk_bf16_f32 v70, v67, v72
	v_cvt_pk_bf16_f32 v67, v68, v69
	v_cndmask_b32_e64 v68, v67, 0, s[12:13]
	v_lshrrev_b32_e32 v67, 16, v67
	v_cndmask_b32_e64 v67, v67, 0, s[10:11]
	v_perm_b32 v71, v67, v68, s0
	ds_write_b64 v110, v[70:71]
	v_mov_b32_e32 v67, 0
	v_mov_b32_e32 v68, 0
	v_mov_b32_e32 v69, 0
	v_mov_b32_e32 v70, 0
	v_mov_b32_e32 v71, 0
	s_cbranch_vccz .LBB0_936
	ds_read_b128 v[68:71], v116 offset:4352
	ds_read_b128 v[72:75], v88 offset:45056
	s_waitcnt lgkmcnt(0)
	v_mfma_f32_16x16x32_bf16 v[68:71], v[68:71], v[72:75], 0
	ds_read_b128 v[72:75], v116 offset:4416
	ds_read_b128 v[128:131], v88 offset:45120
	s_waitcnt lgkmcnt(0)
	v_mfma_f32_16x16x32_bf16 v[68:71], v[72:75], v[128:131], v[68:71]
	ds_read_b128 v[72:75], v116 offset:4480
	ds_read_b128 v[128:131], v88 offset:45184
	s_waitcnt lgkmcnt(0)
	v_mfma_f32_16x16x32_bf16 v[68:71], v[72:75], v[128:131], v[68:71]
	ds_read_b128 v[72:75], v116 offset:4544
	ds_read_b128 v[128:131], v88 offset:45248
	s_waitcnt lgkmcnt(0)
	v_mfma_f32_16x16x32_bf16 v[68:71], v[72:75], v[128:131], v[68:71]
	ds_read_b128 v[72:75], v89 offset:64
	s_waitcnt lgkmcnt(0)
	v_sub_f32_e32 v72, v72, v41
	v_sub_f32_e32 v73, v73, v41
	v_sub_f32_e32 v74, v74, v41
	v_sub_f32_e32 v75, v75, v41
	v_mul_f32_e32 v72, 0x3fb8aa3b, v72
	v_mul_f32_e32 v73, 0x3fb8aa3b, v73
	v_mul_f32_e32 v74, 0x3fb8aa3b, v74
	v_mul_f32_e32 v75, 0x3fb8aa3b, v75
	v_exp_f32_e32 v72, v72
	v_exp_f32_e32 v73, v73
	v_exp_f32_e32 v74, v74
	v_exp_f32_e32 v75, v75
	v_pk_mul_f32 v[68:69], v[68:69], v[72:73]
	s_nop 0
	v_cndmask_b32_e64 v68, v68, 0, s[20:21]
	v_pk_mul_f32 v[70:71], v[70:71], v[74:75]
	v_cndmask_b32_e64 v69, v69, 0, s[18:19]
	v_cndmask_b32_e64 v70, v70, 0, s[16:17]
	v_cndmask_b32_e64 v71, v71, 0, s[14:15]

; #define LAS __attribute__((address_space(3)))
; __device__ __forceinline__ unsigned long long pack4bf(f32x4 v) { return (unsigned long long)pk2(v[0], v[1]) | ((unsigned long long)pk2(v[2], v[3]) << 32); }
; __device__ __forceinline__ void rwkv_chunk_unit(Frame& F, int unit, LAS unsigned char* regB, LAS unsigned* bcnt, unsigned& btarget) {
;     ...
;         { yv = __builtin_amdgcn_mfma_f32_16x16x32_bf16(*(const LAS s16x8*)(G3b + (16 * mi + fr) * LS + 8 * fq), *(const LAS s16x8*)(Ubt + (16 * nj + fr) * LS + 8 * fq), yv, 0, 0, 0);
;           float* yp = YRAW + ((size_t)b * SEQ + ch * 32 + 16 * mi + 4 * fq) * RD + h * 64 + half * 32 + 16 * nj + fr;
; #pragma unroll
;           for (int rg_ = 0; rg_ < 4; ++rg_) yp[(size_t)rg_ * RD] = yv[rg_]; }
;         { const int kt = w; const s16x8 bt_ = tr_frag(Bt, KS, 8 * fq, 16 * kt, fr), kt_ = tr_frag(Kt, KS, 8 * fq, 16 * kt, fr); const f32x4 gl4 = *(const LAS f32x4*)(glf + 16 * kt + 4 * fq);
; #pragma unroll
;           for (int vt = 0; vt < 2; ++vt) {
;               st[vt] = __builtin_amdgcn_mfma_f32_16x16x32_bf16(bt_, *(const LAS s16x8*)(Ubt + (16 * vt + fr) * LS + 8 * fq), st[vt], 0, 0, 0);
;               st[vt] = __builtin_amdgcn_mfma_f32_16x16x32_bf16(kt_, tr_frag(Vv, LS, 8 * fq, 16 * vt, fr), st[vt], 0, 0, 0);
;               st[vt] = st[vt] * gl4;
;               *(LAS unsigned long long*)(Sb + (16 * vt + fr) * KS + 16 * kt + 4 * fq) = pack4bf(st[vt]); } }
.LBB0_989:
	s_waitcnt vmcnt(2)
	ds_read_b128 v[6:9], v173 offset:28160
	ds_read_b128 v[10:13], v177
	s_cmp_lg_u32 s18, 64
	s_mov_b32 s10, s18
	s_waitcnt lgkmcnt(0)
	v_mfma_f32_16x16x32_bf16 v[2:5], v[6:9], v[10:13], v[2:5]
	v_lshl_add_u64 v[6:7], v[160:161], 0, s[0:1]
	v_lshlrev_b64 v[6:7], 12, v[6:7]
	v_lshl_add_u64 v[6:7], v[164:165], 0, v[6:7]
	v_add_co_u32_e32 v8, vcc, 0x1000, v6
	s_nop 3
	global_store_dword v[6:7], v2, off
	v_addc_co_u32_e32 v9, vcc, 0, v7, vcc
	v_add_co_u32_e32 v2, vcc, 0x2000, v6
	global_store_dword v[8:9], v3, off
	s_nop 0
	v_addc_co_u32_e32 v3, vcc, 0, v7, vcc
	global_store_dword v[2:3], v4, off
	v_add_co_u32_e32 v2, vcc, 0x3000, v6
	s_nop 1
	v_addc_co_u32_e32 v3, vcc, 0, v7, vcc
	global_store_dword v[2:3], v5, off
	ds_read_b64_tr_b16 v[2:3], v178 offset:4608
	ds_read_b64_tr_b16 v[4:5], v178 offset:5184
	ds_read_b64_tr_b16 v[6:7], v178 offset:9216
	ds_read_b64_tr_b16 v[8:9], v178 offset:9792
	ds_read_b128 v[10:13], v179
	ds_read_b128 v[14:17], v190
	ds_read_b64_tr_b16 v[18:19], v171 offset:18432
	ds_read_b64_tr_b16 v[20:21], v171 offset:18752
	s_waitcnt lgkmcnt(2)
	v_mfma_f32_16x16x32_bf16 v[14:17], v[2:5], v[14:17], v[90:93]
	s_waitcnt lgkmcnt(0)
	v_mfma_f32_16x16x32_bf16 v[14:17], v[6:9], v[18:21], v[14:17]
	v_lshlrev_b32_e32 v18, 16, v241
	v_and_b32_e32 v19, 0xffff0000, v241
	s_nop 5
	v_pk_mul_f32 v[92:93], v[12:13], v[16:17]
	v_pk_mul_f32 v[90:91], v[10:11], v[14:15]
	v_cvt_pk_bf16_f32 v15, v92, v93
	v_cvt_pk_bf16_f32 v14, v90, v91
	ds_write_b64 v191, v[14:15] offset:20992
	ds_read_b128 v[14:17], v192
	s_waitcnt lgkmcnt(0)
	v_mfma_f32_16x16x32_bf16 v[2:5], v[2:5], v[14:17], v[78:81]
	ds_read_b64_tr_b16 v[14:15], v171 offset:18464
	ds_read_b64_tr_b16 v[16:17], v171 offset:18784
	s_waitcnt lgkmcnt(0)
	v_mfma_f32_16x16x32_bf16 v[2:5], v[6:9], v[14:17], v[2:5]
	v_lshlrev_b32_e32 v14, 16, v243
	v_and_b32_e32 v15, 0xffff0000, v243
	v_lshlrev_b32_e32 v16, 16, v240
	s_nop 4
	v_pk_mul_f32 v[80:81], v[12:13], v[4:5]
	v_pk_mul_f32 v[78:79], v[10:11], v[2:3]
	v_cvt_pk_bf16_f32 v3, v80, v81
	v_cvt_pk_bf16_f32 v2, v78, v79
	v_lshlrev_b32_e32 v12, 16, v242
	v_and_b32_e32 v13, 0xffff0000, v242
	v_and_b32_e32 v17, 0xffff0000, v240
	ds_write_b64 v191, v[2:3] offset:23296
	s_cbranch_scc0 .LBB0_967

; #define LAS __attribute__((address_space(3)))
; __device__ __forceinline__ void rwkv_chunk_unit(Frame& F, int unit, LAS unsigned char* regB, LAS unsigned* bcnt, unsigned& btarget) {
;     ...
;         { const int tq = lane & 31, hq = lane >> 5; f32x4 c0v, c1v;
; #pragma unroll
;           for (int j = 0; j < 4; ++j) { c0v[j] = scan32(ws0[j]); c1v[j] = scan32(ws1[j]); }
;           *(LAS f32x4*)(csf + tq * 64 + 16 * w + 8 * hq) = c0v; *(LAS f32x4*)(csf + tq * 64 + 16 * w + 8 * hq + 4) = c1v; }
;         if (ch + 1 < SEQ / 32) RC_LOAD(ch + 1);
.LBB0_994:
	s_or_b64 exec, exec, s[4:5]
	s_waitcnt vmcnt(2)
	v_mov_b32_dpp v2, v86 row_shr:1 row_mask:0xf bank_mask:0xf bound_ctrl:1
	v_mov_b32_dpp v3, v87 row_shr:1 row_mask:0xf bank_mask:0xf bound_ctrl:1
	v_mov_b32_dpp v4, v82 row_shr:1 row_mask:0xf bank_mask:0xf bound_ctrl:1
	v_pk_add_f32 v[2:3], v[86:87], v[2:3]
	v_mov_b32_dpp v5, v83 row_shr:1 row_mask:0xf bank_mask:0xf bound_ctrl:1
	v_pk_add_f32 v[4:5], v[82:83], v[4:5]
	v_mov_b32_dpp v6, v2 row_shr:2 row_mask:0xf bank_mask:0xf bound_ctrl:1
	v_mov_b32_dpp v7, v3 row_shr:2 row_mask:0xf bank_mask:0xf bound_ctrl:1
	v_pk_add_f32 v[2:3], v[2:3], v[6:7]
	v_mov_b32_dpp v8, v4 row_shr:2 row_mask:0xf bank_mask:0xf bound_ctrl:1
	v_mov_b32_dpp v9, v5 row_shr:2 row_mask:0xf bank_mask:0xf bound_ctrl:1
	v_mov_b32_dpp v6, v2 row_shr:4 row_mask:0xf bank_mask:0xf bound_ctrl:1
	v_mov_b32_dpp v7, v3 row_shr:4 row_mask:0xf bank_mask:0xf bound_ctrl:1
	v_pk_add_f32 v[4:5], v[4:5], v[8:9]
	v_pk_add_f32 v[2:3], v[2:3], v[6:7]
	v_mov_b32_e32 v196, 0
	v_mov_b32_dpp v8, v4 row_shr:4 row_mask:0xf bank_mask:0xf bound_ctrl:1
	v_mov_b32_dpp v9, v5 row_shr:4 row_mask:0xf bank_mask:0xf bound_ctrl:1
	v_mov_b32_dpp v6, v2 row_shr:8 row_mask:0xf bank_mask:0xf bound_ctrl:1
	v_mov_b32_dpp v7, v3 row_shr:8 row_mask:0xf bank_mask:0xf bound_ctrl:1
	v_pk_add_f32 v[4:5], v[4:5], v[8:9]
	v_pk_add_f32 v[2:3], v[2:3], v[6:7]
	v_mov_b32_e32 v6, 0
	v_mov_b32_e32 v7, 0
	v_mov_b32_dpp v8, v4 row_shr:8 row_mask:0xf bank_mask:0xf bound_ctrl:1
	v_mov_b32_dpp v9, v5 row_shr:8 row_mask:0xf bank_mask:0xf bound_ctrl:1
	v_mov_b32_dpp v6, v2 row_bcast:15 row_mask:0xa bank_mask:0xf
	v_mov_b32_dpp v7, v3 row_bcast:15 row_mask:0xa bank_mask:0xf
	v_pk_add_f32 v[10:11], v[4:5], v[8:9]
	v_mov_b32_dpp v4, v88 row_shr:1 row_mask:0xf bank_mask:0xf bound_ctrl:1
	v_mov_b32_dpp v8, v84 row_shr:1 row_mask:0xf bank_mask:0xf bound_ctrl:1
	v_mov_b32_dpp v5, v89 row_shr:1 row_mask:0xf bank_mask:0xf bound_ctrl:1
	v_mov_b32_dpp v9, v85 row_shr:1 row_mask:0xf bank_mask:0xf bound_ctrl:1
	v_pk_add_f32 v[4:5], v[88:89], v[4:5]
	v_pk_add_f32 v[2:3], v[2:3], v[6:7]
	v_pk_add_f32 v[6:7], v[84:85], v[8:9]
	v_mov_b32_dpp v198, v4 row_shr:2 row_mask:0xf bank_mask:0xf bound_ctrl:1
	v_mov_b32_dpp v199, v5 row_shr:2 row_mask:0xf bank_mask:0xf bound_ctrl:1
	v_mov_b32_dpp v8, v6 row_shr:2 row_mask:0xf bank_mask:0xf bound_ctrl:1
	v_mov_b32_dpp v9, v7 row_shr:2 row_mask:0xf bank_mask:0xf bound_ctrl:1
	v_pk_add_f32 v[4:5], v[4:5], v[198:199]
	v_pk_add_f32 v[6:7], v[6:7], v[8:9]
	v_mov_b32_e32 v197, 0
	v_mov_b32_dpp v198, v4 row_shr:4 row_mask:0xf bank_mask:0xf bound_ctrl:1
	v_mov_b32_dpp v199, v5 row_shr:4 row_mask:0xf bank_mask:0xf bound_ctrl:1
	v_mov_b32_dpp v8, v6 row_shr:4 row_mask:0xf bank_mask:0xf bound_ctrl:1
	v_mov_b32_dpp v9, v7 row_shr:4 row_mask:0xf bank_mask:0xf bound_ctrl:1
	v_pk_add_f32 v[4:5], v[4:5], v[198:199]
	v_pk_add_f32 v[6:7], v[6:7], v[8:9]
	v_mov_b32_dpp v196, v10 row_bcast:15 row_mask:0xa bank_mask:0xf
	v_mov_b32_dpp v198, v4 row_shr:8 row_mask:0xf bank_mask:0xf bound_ctrl:1
	v_mov_b32_dpp v199, v5 row_shr:8 row_mask:0xf bank_mask:0xf bound_ctrl:1
	v_mov_b32_dpp v8, v6 row_shr:8 row_mask:0xf bank_mask:0xf bound_ctrl:1
	v_mov_b32_dpp v9, v7 row_shr:8 row_mask:0xf bank_mask:0xf bound_ctrl:1
	v_pk_add_f32 v[4:5], v[4:5], v[198:199]
	v_mov_b32_e32 v198, 0
	v_mov_b32_e32 v199, 0
	v_pk_add_f32 v[6:7], v[6:7], v[8:9]
	v_mov_b32_e32 v8, 0
	v_mov_b32_e32 v9, 0
	v_mov_b32_dpp v197, v11 row_bcast:15 row_mask:0xa bank_mask:0xf
	v_mov_b32_dpp v198, v4 row_bcast:15 row_mask:0xa bank_mask:0xf
	v_mov_b32_dpp v199, v5 row_bcast:15 row_mask:0xa bank_mask:0xf
	v_mov_b32_dpp v8, v6 row_bcast:15 row_mask:0xa bank_mask:0xf
	v_mov_b32_dpp v9, v7 row_bcast:15 row_mask:0xa bank_mask:0xf
	s_add_i32 s18, s10, 1
	v_pk_add_f32 v[4:5], v[4:5], v[198:199]
	v_pk_add_f32 v[8:9], v[6:7], v[8:9]
	v_pk_add_f32 v[6:7], v[10:11], v[196:197]
	s_cmp_eq_u32 s10, 63
	ds_write_b128 v99, v[2:5]
	ds_write_b128 v99, v[6:9] offset:16
	s_cbranch_scc1 .LBB0_996
	s_lshl_b32 s96, s18, 5
	v_or_b32_e32 v96, s96, v94
	v_lshl_add_u64 v[2:3], s[94:95], 0, v[96:97]
	v_mad_u64_u32 v[4:5], s[4:5], v2, s33, v[124:125]
	v_mad_i32_i24 v5, v3, s33, v5
	v_add_co_u32_e32 v6, vcc, 0x1000, v4
	global_load_dwordx2 v[128:129], v[4:5], off
	global_load_dwordx2 v[130:131], v[4:5], off offset:2048
	v_addc_co_u32_e32 v7, vcc, 0, v5, vcc
	global_load_dwordx2 v[132:133], v[6:7], off
	v_add_co_u32_e32 v6, vcc, 0xffffb000, v4
	v_lshlrev_b64 v[2:3], 12, v[2:3]
	s_nop 0
	v_addc_co_u32_e32 v7, vcc, -1, v5, vcc
	v_add_co_u32_e32 v4, vcc, 0xffffc000, v4
	v_lshl_add_u64 v[2:3], v[134:135], 0, v[2:3]
	s_nop 0
	v_addc_co_u32_e32 v5, vcc, -1, v5, vcc
	global_load_dwordx2 v[136:137], v[6:7], off offset:-1024
	global_load_dwordx2 v[140:141], v[4:5], off offset:-3072
	global_load_dwordx2 v[138:139], v[4:5], off offset:-1024
	v_add_u32_e32 v96, 16, v96
	global_load_dwordx2 v[240:241], v[2:3], off
	s_mov_b32 s97, s1
	v_lshl_add_u64 v[2:3], s[94:95], 0, v[96:97]
	v_mad_u64_u32 v[4:5], s[4:5], v2, s33, v[124:125]
	s_movk_i32 s4, 0x1000
	v_mad_i32_i24 v5, v3, s33, v5
	v_add_co_u32_e32 v6, vcc, s4, v4
	s_movk_i32 s4, 0xb000
	s_nop 0
	v_addc_co_u32_e32 v7, vcc, 0, v5, vcc
	global_load_dwordx2 v[144:145], v[4:5], off
	global_load_dwordx2 v[146:147], v[4:5], off offset:2048
	global_load_dwordx2 v[148:149], v[6:7], off
	v_add_co_u32_e32 v6, vcc, s4, v4
	s_movk_i32 s4, 0xc000
	s_nop 0
	v_addc_co_u32_e32 v7, vcc, -1, v5, vcc
	v_add_co_u32_e32 v4, vcc, s4, v4
	v_lshlrev_b64 v[2:3], 12, v[2:3]
	s_nop 0
	v_addc_co_u32_e32 v5, vcc, -1, v5, vcc
	v_lshl_add_u64 v[2:3], v[134:135], 0, v[2:3]
	global_load_dwordx2 v[150:151], v[6:7], off offset:-1024
	global_load_dwordx2 v[154:155], v[4:5], off offset:-3072
	global_load_dwordx2 v[158:159], v[4:5], off offset:-1024
	s_nop 0
	global_load_dwordx2 v[242:243], v[2:3], off
	v_lshl_add_u64 v[2:3], v[142:143], 0, s[96:97]
	v_lshlrev_b64 v[2:3], 12, v[2:3]
	v_lshl_add_u64 v[2:3], v[156:157], 0, v[2:3]
	global_load_dwordx4 v[82:85], v[2:3], off offset:16
	global_load_dwordx4 v[86:89], v[2:3], off

; __global__ void __launch_bounds__(NTHR, 2) mk_fwd(Args args) {
	.amdhsa_kernel _Z6mk_fwd4Args
		.amdhsa_group_segment_fixed_size 0
		.amdhsa_private_segment_fixed_size 0
		.amdhsa_kernarg_size 520
		.amdhsa_user_sgpr_count 2
		.amdhsa_user_sgpr_dispatch_ptr 0
		.amdhsa_user_sgpr_queue_ptr 0
		.amdhsa_user_sgpr_kernarg_segment_ptr 1
		.amdhsa_user_sgpr_dispatch_id 0
		.amdhsa_user_sgpr_kernarg_preload_length 0
		.amdhsa_user_sgpr_kernarg_preload_offset 0
		.amdhsa_user_sgpr_private_segment_size 0
		.amdhsa_uses_dynamic_stack 0
		.amdhsa_enable_private_segment 0
		.amdhsa_system_sgpr_workgroup_id_x 1
		.amdhsa_system_sgpr_workgroup_id_y 0
		.amdhsa_system_sgpr_workgroup_id_z 0
		.amdhsa_system_sgpr_workgroup_info 0
		.amdhsa_system_vgpr_workitem_id 0
		.amdhsa_next_free_vgpr 248
		.amdhsa_next_free_sgpr 98
		.amdhsa_accum_offset 248
		.amdhsa_reserve_vcc 1
		.amdhsa_float_round_mode_32 0
		.amdhsa_float_round_mode_16_64 0
		.amdhsa_float_denorm_mode_32 3
		.amdhsa_float_denorm_mode_16_64 3
		.amdhsa_dx10_clamp 1
		.amdhsa_ieee_mode 1
		.amdhsa_fp16_overflow 0
		.amdhsa_tg_split 0
		.amdhsa_exception_fp_ieee_invalid_op 0
		.amdhsa_exception_fp_denorm_src 0
		.amdhsa_exception_fp_ieee_div_zero 0
		.amdhsa_exception_fp_ieee_overflow 0
		.amdhsa_exception_fp_ieee_underflow 0
		.amdhsa_exception_fp_ieee_inexact 0
		.amdhsa_exception_int_div_zero 0
	.end_amdhsa_kernel

; __global__ void __launch_bounds__(NTHR, 2) mk_fwd(Args args) {
amdhsa.kernels:
  - .agpr_count:     0
    .args:
      - .offset:         0
        .size:           264
        .value_kind:     by_value
      - .offset:         264
        .size:           4
        .value_kind:     hidden_block_count_x
      - .offset:         268
        .size:           4
        .value_kind:     hidden_block_count_y
      - .offset:         272
        .size:           4
        .value_kind:     hidden_block_count_z
      - .offset:         276
        .size:           2
        .value_kind:     hidden_group_size_x
      - .offset:         278
        .size:           2
        .value_kind:     hidden_group_size_y
      - .offset:         280
        .size:           2
        .value_kind:     hidden_group_size_z
      - .offset:         282
        .size:           2
        .value_kind:     hidden_remainder_x
      - .offset:         284
        .size:           2
        .value_kind:     hidden_remainder_y
      - .offset:         286
        .size:           2
        .value_kind:     hidden_remainder_z
      - .offset:         304
        .size:           8
        .value_kind:     hidden_global_offset_x
      - .offset:         312
        .size:           8
        .value_kind:     hidden_global_offset_y
      - .offset:         320
        .size:           8
        .value_kind:     hidden_global_offset_z
      - .offset:         328
        .size:           2
        .value_kind:     hidden_grid_dims
      - .offset:         384
        .size:           4
        .value_kind:     hidden_dynamic_lds_size
    .group_segment_fixed_size: 0
    .kernarg_segment_align: 8
    .kernarg_segment_size: 520
    .language:       OpenCL C
    .language_version:
      - 2
      - 0
    .max_flat_workgroup_size: 512
    .name:           _Z6mk_fwd4Args
    .private_segment_fixed_size: 0
    .sgpr_count:     104
    .sgpr_spill_count: 126
    .symbol:         _Z6mk_fwd4Args.kd
    .uniform_work_group_size: 1
    .uses_dynamic_stack: false
    .vgpr_count:     248
    .vgpr_spill_count: 0
    .wavefront_size: 64
